# speedup vs baseline: 1.0046x; 1.0046x over previous
.LBB2_4:
	s_or_b64 exec, exec, s[4:5]
	s_and_b64 s[2:3], s[2:3], exec
	s_cselect_b32 s10, s6, 0x752
	s_lshl_b32 s33, s10, 4
	s_add_i32 s2, s33, 0x7530
	v_or_b32_e32 v110, s2, v115
	v_mov_b32_e32 v111, 0
	s_waitcnt lgkmcnt(0)
	v_bfe_u32 v4, v0, 4, 2
	v_mul_u32_u24_e32 v4, 0x1d4c0, v4
	v_mov_b32_e32 v5, 0
	v_lshl_add_u64 v[2:3], v[110:111], 1, s[24:25]
	v_lshl_add_u64 v[2:3], v[2:3], 0, v[4:5]
	global_load_ushort v1, v[2:3], off
	s_mov_b64 s[4:5], 0x75300
	v_lshl_add_u64 v[2:3], v[2:3], 0, s[4:5]
	global_load_ushort v199, v[2:3], off
	s_load_dwordx2 s[30:31], s[0:1], 0x20
	v_and_b32_e32 v110, 63, v0
	v_cmp_lt_u32_e32 vcc, 37, v110
	s_mul_hi_i32 s27, s10, 38
	s_mul_i32 s26, s10, 38
	s_and_saveexec_b64 s[2:3], vcc
	s_xor_b64 s[2:3], exec, s[2:3]
	s_add_i32 s4, s10, 1
	s_ashr_i32 s5, s4, 31
	s_mul_hi_i32 s7, s4, 38
	s_mul_i32 s6, s4, 38
	s_or_saveexec_b64 s[2:3], s[2:3]
	s_load_dwordx2 s[34:35], s[0:1], 0x28
	v_mov_b64_e32 v[112:113], s[6:7]
	v_mov_b64_e32 v[2:3], s[4:5]
	s_xor_b64 exec, exec, s[2:3]
	s_cbranch_execz .LBB2_8
	v_mov_b32_e32 v111, 0
	v_lshl_add_u64 v[2:3], s[26:27], 0, v[110:111]
	v_lshlrev_b64 v[2:3], 6, v[2:3]
	s_waitcnt lgkmcnt(0)
	v_lshl_add_u64 v[18:19], s[30:31], 0, v[2:3]
	s_add_i32 s4, s10, 1
	global_load_dwordx4 v[2:5], v[18:19], off offset:16
	global_load_dwordx4 v[6:9], v[18:19], off
	global_load_dwordx4 v[10:13], v[18:19], off offset:48
	global_load_dwordx4 v[14:17], v[18:19], off offset:32
	v_mad_i64_i32 v[18:19], s[6:7], s4, 38, v[110:111]
	v_lshlrev_b64 v[18:19], 6, v[18:19]
	v_lshl_add_u64 v[34:35], s[30:31], 0, v[18:19]
	global_load_dwordx4 v[18:21], v[34:35], off
	global_load_dwordx4 v[22:25], v[34:35], off offset:16
	global_load_dwordx4 v[26:29], v[34:35], off offset:32
	global_load_dwordx4 v[30:33], v[34:35], off offset:48
	s_ashr_i32 s5, s4, 31
	s_mul_hi_i32 s7, s4, 38
	s_mul_i32 s6, s4, 38
	v_mov_b64_e32 v[112:113], s[6:7]
	s_waitcnt vmcnt(7)
	v_add_u32_e32 v2, v2, v3
	s_waitcnt vmcnt(6)
	v_add_u32_e32 v6, v6, v7
	v_add3_u32 v6, v6, v8, v9
	v_add3_u32 v2, v2, v4, v5
	s_waitcnt vmcnt(4)
	v_add_u32_e32 v3, v14, v15
	s_waitcnt vmcnt(3)
	v_sub_u32_e32 v5, v18, v6
	v_add_u32_e32 v5, v5, v19
	v_add3_u32 v5, v5, v20, v21
	v_sub_u32_e32 v2, v5, v2
	s_waitcnt vmcnt(2)
	v_add3_u32 v2, v2, v22, v23
	v_add3_u32 v3, v3, v16, v17
	v_add3_u32 v2, v2, v24, v25
	v_sub_u32_e32 v2, v2, v3
	v_add_u32_e32 v7, v10, v11
	s_waitcnt vmcnt(1)
	v_add3_u32 v2, v2, v26, v27
	v_add3_u32 v4, v7, v12, v13
	v_add3_u32 v2, v2, v28, v29
	v_sub_u32_e32 v2, v2, v4
	s_waitcnt vmcnt(0)
	v_add_u32_e32 v2, v2, v30
	v_add3_u32 v2, v2, v31, v32
	v_add3_u32 v2, v2, v33, 16
	v_min_i32_e32 v111, 0x300, v2
	v_mov_b64_e32 v[2:3], s[4:5]

.LBB2_56:
	v_add_u32_e32 v228, 0, v110
	v_lshrrev_b32_e32 v229, 3, v228
	v_and_b32_e32 v228, 7, v228
	v_lshlrev_b32_e32 v228, 4, v228
	v_lshl_or_b32 v228, v229, 8, v228
	global_load_dwordx4 v[208:211], v228, s[58:59]
	v_add_u32_e32 v228, 64, v110
	v_lshrrev_b32_e32 v229, 3, v228
	v_and_b32_e32 v228, 7, v228
	v_lshlrev_b32_e32 v228, 4, v228
	v_lshl_or_b32 v228, v229, 8, v228
	global_load_dwordx4 v[212:215], v228, s[58:59]
	v_add_u32_e32 v228, 128, v110
	v_lshrrev_b32_e32 v229, 3, v228
	v_and_b32_e32 v228, 7, v228
	v_lshlrev_b32_e32 v228, 4, v228
	v_lshl_or_b32 v228, v229, 8, v228
	global_load_dwordx4 v[216:219], v228, s[58:59]
	v_add_u32_e32 v228, 192, v110
	v_lshrrev_b32_e32 v229, 3, v228
	v_and_b32_e32 v228, 7, v228
	v_lshlrev_b32_e32 v228, 4, v228
	v_lshl_or_b32 v228, v229, 8, v228
	global_load_dwordx4 v[220:223], v228, s[58:59]
	v_add_u32_e32 v228, 256, v110
	v_lshrrev_b32_e32 v229, 3, v228
	v_and_b32_e32 v228, 7, v228
	v_lshlrev_b32_e32 v228, 4, v228
	v_lshl_or_b32 v228, v229, 8, v228
	global_load_dwordx4 v[224:227], v228, s[58:59]
	v_lshlrev_b32_e32 v228, 4, v110
	v_add_u32_e32 v228, 0x26000, v228
	s_waitcnt vmcnt(0)
	ds_write_b128 v228, v[208:211]
	ds_write_b128 v228, v[212:215] offset:1024
	ds_write_b128 v228, v[216:219] offset:2048
	ds_write_b128 v228, v[220:223] offset:3072
	ds_write_b128 v228, v[224:227] offset:4096
	v_cvt_f32_f16_e32 v197, v1
	v_mov_b32_e32 v185, 0xff61b1e6
	v_mov_b32_e32 v195, 0xff61b1e6
	s_waitcnt lgkmcnt(0)
	s_barrier
.LBB2_58:
	v_mov_b32_e32 v187, 0x4138aa3b
	v_lshrrev_b32_e32 v38, 3, v115
	v_lshlrev_b32_e32 v40, 5, v0
	v_lshrrev_b32_e32 v107, 4, v110
	s_lshl_b32 s6, s38, 13
	v_and_or_b32 v38, v175, 2, v38
	v_and_b32_e32 v40, 0x180, v40
	v_lshlrev_b32_e32 v41, 3, v0
	s_add_i32 s6, s6, 0x12000
	v_lshlrev_b32_e32 v39, 9, v107
	v_and_or_b32 v40, v41, 24, v40
	v_lshlrev_b32_e32 v38, 5, v38
	v_lshrrev_b32_e32 v37, 3, v0
	v_or3_b32 v39, v40, v39, s6
	v_xor_b32_e32 v40, 32, v38
	v_lshl_add_u32 v191, v110, 5, s39
	v_and_b32_e32 v0, 7, v0
	v_or_b32_e32 v186, v39, v38
	v_or_b32_e32 v188, v39, v40
	v_xor_b32_e32 v40, 64, v38
	v_xor_b32_e32 v38, 0x60, v38
	v_bitop3_b32 v0, v37, v0, 6 bitop3:0x6c
	v_or_b32_e32 v190, v39, v38
	v_and_b32_e32 v1, 0x380, v122
	v_lshlrev_b32_e32 v38, 4, v0
	v_add_u32_e32 v0, s33, v115
	v_or_b32_e32 v189, v39, v40
	v_lshlrev_b32_e32 v34, 2, v34
	v_mov_b32_e32 v35, 0
	v_and_b32_e32 v122, 6, v115
	v_xor_b32_e32 v122, v122, v107
	v_lshlrev_b32_e32 v122, 4, v122
	v_lshl_add_u32 v122, v115, 7, v122
	v_add_u32_e32 v122, s6, v122
	s_mov_b32 s60, 0xffff0000
	s_mov_b32 s61, 0
	s_mov_b32 s62, 0
	s_mov_b32 s63, 0xffff
	s_mov_b32 s64, 0
	s_mov_b32 s65, 0xffff0000
	v_or_b32_e32 v39, s6, v1
	v_add_u32_e32 v192, 0x15f90, v0
	v_lshlrev_b32_e32 v0, 7, v107
	v_and_b32_e32 v1, 0x78, v41
	v_lshl_add_u64 v[126:127], s[30:31], 0, v[34:35]
	v_and_b32_e32 v200, 1, v114
	v_mul_u32_u24_e32 v200, 0x980, v200
	v_add_co_u32_e32 v126, vcc, v126, v200
	s_nop 1
	v_addc_co_u32_e32 v127, vcc, 0, v127, vcc
	v_or3_b32 v193, v1, v0, s39
	v_add_u32_e32 v0, s33, v110
	v_mov_b32_e32 v34, v116
	v_mov_b32_e32 v37, v35
	v_lshl_or_b32 v194, v110, 16, v0
	v_lshl_add_u64 v[0:1], v[34:35], 0, v[36:37]
	v_mov_b32_e32 v36, v35
	v_mov_b32_e32 v76, v35
	v_mov_b32_e32 v77, v35
	v_lshl_add_u64 v[0:1], s[34:35], 0, v[0:1]
	v_mov_b32_e32 v34, v35
	v_mov_b32_e32 v74, v35
	v_mov_b32_e32 v75, v35
	s_mov_b32 s12, 0x3c003c00
	v_mov_b64_e32 v[80:81], v[76:77]
	v_mov_b64_e32 v[84:85], v[76:77]
	v_mov_b64_e32 v[88:89], v[76:77]
	v_mov_b64_e32 v[92:93], v[76:77]
	v_mov_b64_e32 v[96:97], v[76:77]
	v_mov_b64_e32 v[100:101], v[76:77]
	v_mov_b64_e32 v[104:105], v[76:77]
	v_mov_b64_e32 v[56:57], v[36:37]
	v_mov_b64_e32 v[60:61], v[36:37]
	v_mov_b64_e32 v[64:65], v[36:37]
	v_mov_b64_e32 v[68:69], v[36:37]
	v_mov_b64_e32 v[72:73], v[36:37]
	s_or_b32 s47, s40, 0x80
	v_lshl_add_u64 v[0:1], v[0:1], 0, 64
	s_mov_b32 s49, 0
	s_mov_b64 s[30:31], -1
	s_mov_b32 s13, s12
	s_movk_i32 s48, 0x300
	v_lshl_add_u32 v118, v114, 4, v116
	v_mov_b32_e32 v119, v165
	v_mov_b32_e32 v116, 0xc3500
	v_lshlrev_b32_e32 v128, 2, v114
	v_add_u32_e32 v196, v39, v38
	v_mov_b64_e32 v[78:79], v[74:75]
	v_mov_b64_e32 v[82:83], v[74:75]
	v_mov_b64_e32 v[86:87], v[74:75]
	v_mov_b64_e32 v[90:91], v[74:75]
	v_mov_b64_e32 v[94:95], v[74:75]
	v_mov_b64_e32 v[98:99], v[74:75]
	v_mov_b64_e32 v[102:103], v[74:75]
	v_mov_b64_e32 v[54:55], v[34:35]
	v_mov_b64_e32 v[58:59], v[34:35]
	v_mov_b64_e32 v[62:63], v[34:35]
	v_mov_b64_e32 v[66:67], v[34:35]
	s_mov_b32 s50, 0
	v_mov_b64_e32 v[70:71], v[34:35]
	v_mov_b32_e32 v50, v35
	v_mov_b32_e32 v51, v35
	v_mov_b32_e32 v52, v35
	v_mov_b32_e32 v53, v35
	v_mov_b32_e32 v46, v35
	v_mov_b32_e32 v47, v35
	v_mov_b32_e32 v48, v35
	v_mov_b32_e32 v49, v35
	v_mov_b32_e32 v42, v35
	v_mov_b32_e32 v43, v35
	v_mov_b32_e32 v44, v35
	v_mov_b32_e32 v45, v35
	v_mov_b32_e32 v38, v35
	v_mov_b32_e32 v39, v35
	v_mov_b32_e32 v40, v35
	v_mov_b32_e32 v41, v35
	s_waitcnt vmcnt(0)
	ds_write_b128 v196, v[10:13]
	ds_write_b128 v196, v[14:17] offset:1024
	ds_write_b128 v196, v[30:33] offset:2048
	ds_write_b128 v196, v[26:29] offset:3072
	ds_write_b128 v196, v[2:5] offset:4096
	ds_write_b128 v196, v[6:9] offset:5120
	ds_write_b128 v196, v[18:21] offset:6144
	ds_write_b128 v196, v[22:25] offset:7168
	s_mul_i32 s78, s42, 0xc00
	s_add_i32 s78, s78, s40
	v_mov_b32_e32 v183, v121
	s_lshl_b32 s6, s43, 6
	s_sub_i32 s83, s44, s6
	s_lshl_b32 s6, s43, 8
	s_add_i32 s82, s78, s6
	v_add_u32_e32 v229, s82, v172
	v_add_u32_e32 v230, s82, v173
	ds_read_u16 v224, v229 offset:0
	ds_read_u16 v225, v229 offset:32
	ds_read_u16 v226, v229 offset:64
	ds_read_u16 v227, v229 offset:96
	ds_read_u16 v232, v229 offset:128
	ds_read_u16 v233, v229 offset:160
	ds_read_u16 v234, v229 offset:192
	ds_read_u16 v235, v229 offset:224
	ds_read_b32 v183, v230
	s_waitcnt lgkmcnt(0)
	s_mov_b32 s85, s83

.LBB2_64:
	v_bfe_u32 v34, v121, 16, 4
	v_cmp_gt_i32_e64 s[56:57], s66, v110
	v_lshl_add_u32 v115, v34, 1, v191
	v_lshl_add_u32 v34, v34, 2, s86
	ds_bpermute_b32 v121, v34, v197
	s_cmp_lt_i32 s66, 33
	s_cbranch_scc1 .Lmk_half_iter
	ds_read_b128 v[208:211], v122
	ds_read_b128 v[212:215], v117
	ds_read_b128 v[216:219], v122 offset:2048
	ds_read_b128 v[220:223], v117 offset:2048
	ds_read_b128 v[224:227], v122 offset:4096
	ds_read_b128 v[228:231], v117 offset:4096
	ds_read_b128 v[232:235], v122 offset:6144
	ds_read_b128 v[236:239], v117 offset:6144
	ds_read_b64_tr_b16 v[130:131], v186 offset:0
	ds_read_b64_tr_b16 v[132:133], v186 offset:2048
	ds_read_b64_tr_b16 v[134:135], v188 offset:0
	ds_read_b64_tr_b16 v[136:137], v188 offset:2048
	ds_read_b64_tr_b16 v[138:139], v189 offset:0
	ds_read_b64_tr_b16 v[140:141], v189 offset:2048
	ds_read_b64_tr_b16 v[142:143], v190 offset:0
	ds_read_b64_tr_b16 v[144:145], v190 offset:2048

.LBB2_105:
	s_lshl_b32 s0, s50, 13
	v_lshl_add_u32 v36, v110, 4, s0
	global_load_dwordx4 v[86:89], v36, s[16:17]
	global_load_dwordx4 v[82:85], v36, s[16:17] offset:1024
	global_load_dwordx4 v[78:81], v36, s[16:17] offset:2048
	global_load_dwordx4 v[74:77], v36, s[16:17] offset:3072
	v_add_u32_e32 v37, 0x1000, v36
	global_load_dwordx4 v[90:93], v37, s[16:17]
	global_load_dwordx4 v[94:97], v37, s[16:17] offset:1024
	global_load_dwordx4 v[98:101], v37, s[16:17] offset:2048
	global_load_dwordx4 v[102:105], v37, s[16:17] offset:3072
	s_and_b32 s0, s50, 3
	s_lshl_b32 s86, s0, 6
	s_cmp_lg_u32 s0, 0
	s_cbranch_scc1 .LBB2_64
	s_cmp_eq_u32 s50, 0
	s_cbranch_scc1 .LBB2_64
	v_cvt_f32_f16_e32 v197, v199
	s_cmp_gt_u32 s50, 33
	s_cbranch_scc1 .LBB2_64
	s_add_i32 s0, s50, 3
	v_add_u32_e32 v34, s0, v107
	v_min_u32_e32 v34, 36, v34
	v_mul_u32_u24_e32 v34, 0x1d4c0, v34
	v_lshl_add_u32 v34, v192, 1, v34
	global_load_ushort v199, v34, s[24:25]
	s_branch .LBB2_64
